# up-GEMM K-loops: removed the back-to-back s_setprio 0/1 between the two MFMA groups of a phase
# speedup vs baseline: 1.0218x; 1.0218x over previous
; #define PG8_STAGE(bufoff, gbase, voff) do { _Pragma("unroll") for (int _i = 0; _i < 2; ++_i) { const char* gb_ = (const char*)(gbase) + _i * rstep; asm volatile("" : "+s"(gb_));   \
;         __builtin_amdgcn_global_load_lds((const unsigned*)(gb_ + (voff)), (LAS unsigned*)(lds + (bufoff) + ldsw + _i * 8192), 16, 0, 0); } } while (0)
; #define PG8_LDA(dst, b, h) do { _Pragma("unroll") for (int m = 0; m < 4; ++m) _Pragma("unroll") for (int k = 0; k < 2; ++k) dst[m][k] = *(const LAS bf16x8*)(lds + PG8_SA(b, h) + aoff + m * 2048 + k * 1024); } while (0)
; #define PG8_LDB(dst, b, h) do { _Pragma("unroll") for (int n = 0; n < 2; ++n) _Pragma("unroll") for (int k = 0; k < 2; ++k) dst[n][k] = *(const LAS bf16x8*)(lds + PG8_SB(b, h) + boff + n * 2048 + k * 1024); } while (0)
; #define PG8_WAIT_V(n) asm volatile("s_waitcnt vmcnt(" #n ")" ::: "memory")
; #define PG8_WAIT_L(n) asm volatile("s_waitcnt lgkmcnt(" #n ")" ::: "memory")
; #define PG8_BAR __builtin_amdgcn_s_barrier()
; #define PG8_SCHED __builtin_amdgcn_sched_barrier(0)
; template <class Epi, class Sched, bool ALIGN_EPI = true, bool SP2 = true, bool I8 = false, bool F8 = false>
; __device__ __forceinline__ void gemm_phase(LAS unsigned char* lds, const int K, const Sched& S, const Epi& E, const int wave) {
;     ...
;             PG8_LDB(B0, 0, 0); PG8_LDB(B1, 0, 1); PG8_SCHED; PG8_LDA(At, 0, 0); PG8_STAGE(PG8_SA(1, 1), a1 + hstep, voffA);
;             PG8_WAIT_V(8); PG8_WAIT_L(0); PG8_BAR; PG8_MMA(0, 0, At, B0); PG8_MMA(0, 1, At, B1); PG8_BAR; PG8_SCHED;
;             PG8_LDA(At, 0, 1); PG8_STAGE(PG8_SB(0, 0), b2, voffB); PG8_STAGE(PG8_SB(0, 1), b2 + hstep, voffB); PG8_STAGE(PG8_SA(0, 0), a2, voffA);
;             PG8_WAIT_V(8); PG8_WAIT_L(0); PG8_BAR; PG8_MMA(1, 0, At, B0); PG8_MMA(1, 1, At, B1); PG8_BAR; PG8_SCHED;
.LBB0_1540:
	s_add_u32 s21, s22, 0xfffd0080
	s_addc_u32 s24, s23, -1
	s_cmp_eq_u32 s19, 4
	s_cselect_b32 s25, s15, s24
	s_cselect_b32 s24, s14, s21
	s_cselect_b32 s28, s16, s11
	s_cselect_b32 s29, s17, s13
	s_add_u32 s26, s24, 0x80
	s_addc_u32 s27, s25, 0
	s_add_i32 s21, 0, 0x10000
	v_add_u32_e32 v132, s21, v135
	s_add_i32 s63, 0, 0x14000
	ds_read_b128 v[136:139], v132
	ds_read_b128 v[140:143], v132 offset:1024
	ds_read_b128 v[146:149], v132 offset:2048
	ds_read_b128 v[150:153], v132 offset:3072
	v_add_u32_e32 v132, s63, v135
	ds_read_b128 v[154:157], v132
	ds_read_b128 v[158:161], v132 offset:1024
	ds_read_b128 v[166:169], v132 offset:2048
	ds_read_b128 v[170:173], v132 offset:3072
	s_add_u32 s68, s22, 0xffff0000
	s_addc_u32 s69, s23, -1
	ds_read_b128 v[174:177], v145
	ds_read_b128 v[178:181], v145 offset:1024
	ds_read_b128 v[182:185], v145 offset:2048
	ds_read_b128 v[186:189], v145 offset:3072
	ds_read_b128 v[190:193], v145 offset:4096
	ds_read_b128 v[194:197], v145 offset:5120
	ds_read_b128 v[198:201], v145 offset:6144
	ds_read_b128 v[202:205], v145 offset:7168
	s_add_i32 m0, s58, 0xc000
	v_lshl_add_u64 v[132:133], s[68:69], 0, v[130:131]
	s_mov_b64 s[68:69], s[22:23]
	global_load_lds_dwordx4 v[132:133], off
	s_add_i32 m0, s58, 0xe000
	v_lshl_add_u64 v[132:133], s[68:69], 0, v[130:131]
	global_load_lds_dwordx4 v[132:133], off
	s_waitcnt vmcnt(8)
	s_waitcnt lgkmcnt(0)
	s_barrier
	s_setprio 1
	s_waitcnt lgkmcnt(0)
	s_cmp_eq_u32 s19, -2
	s_cbranch_scc1 .Lzmu_s0
	v_mfma_i32_16x16x64_i8 v[126:129], v[136:139], v[174:177], v[126:129]
	v_mfma_i32_16x16x64_i8 v[118:121], v[146:149], v[174:177], v[118:121]
	v_mfma_i32_16x16x64_i8 v[108:111], v[136:139], v[182:185], v[108:111]
	v_mfma_i32_16x16x64_i8 v[100:103], v[146:149], v[182:185], v[100:103]
	v_mfma_i32_16x16x64_i8 v[92:95], v[136:139], v[190:193], v[92:95]
	v_mfma_i32_16x16x64_i8 v[84:87], v[146:149], v[190:193], v[84:87]
	v_mfma_i32_16x16x64_i8 v[76:79], v[136:139], v[198:201], v[76:79]
	v_mfma_i32_16x16x64_i8 v[68:71], v[146:149], v[198:201], v[68:71]
	v_mfma_i32_16x16x64_i8 v[126:129], v[140:143], v[178:181], v[126:129]
	v_mfma_i32_16x16x64_i8 v[118:121], v[150:153], v[178:181], v[118:121]
	v_mfma_i32_16x16x64_i8 v[108:111], v[140:143], v[186:189], v[108:111]
	v_mfma_i32_16x16x64_i8 v[100:103], v[150:153], v[186:189], v[100:103]
	v_mfma_i32_16x16x64_i8 v[92:95], v[140:143], v[194:197], v[92:95]
	v_mfma_i32_16x16x64_i8 v[84:87], v[150:153], v[194:197], v[84:87]
	v_mfma_i32_16x16x64_i8 v[76:79], v[140:143], v[202:205], v[76:79]
	v_mfma_i32_16x16x64_i8 v[68:71], v[150:153], v[202:205], v[68:71]
	v_mfma_i32_16x16x64_i8 v[122:125], v[154:157], v[174:177], v[122:125]
	v_mfma_i32_16x16x64_i8 v[114:117], v[166:169], v[174:177], v[114:117]
	v_mfma_i32_16x16x64_i8 v[104:107], v[154:157], v[182:185], v[104:107]
	v_mfma_i32_16x16x64_i8 v[96:99], v[166:169], v[182:185], v[96:99]
	v_mfma_i32_16x16x64_i8 v[88:91], v[154:157], v[190:193], v[88:91]
	v_mfma_i32_16x16x64_i8 v[80:83], v[166:169], v[190:193], v[80:83]
	v_mfma_i32_16x16x64_i8 v[72:75], v[154:157], v[198:201], v[72:75]
	v_mfma_i32_16x16x64_i8 v[64:67], v[166:169], v[198:201], v[64:67]
	v_mfma_i32_16x16x64_i8 v[122:125], v[158:161], v[178:181], v[122:125]
	v_mfma_i32_16x16x64_i8 v[114:117], v[170:173], v[178:181], v[114:117]
	v_mfma_i32_16x16x64_i8 v[104:107], v[158:161], v[186:189], v[104:107]
	v_mfma_i32_16x16x64_i8 v[96:99], v[170:173], v[186:189], v[96:99]
	v_mfma_i32_16x16x64_i8 v[88:91], v[158:161], v[194:197], v[88:91]
	v_mfma_i32_16x16x64_i8 v[80:83], v[170:173], v[194:197], v[80:83]
	v_mfma_i32_16x16x64_i8 v[72:75], v[158:161], v[202:205], v[72:75]
	v_mfma_i32_16x16x64_i8 v[64:67], v[170:173], v[202:205], v[64:67]
	s_setprio 0
.Lzmu_r0:
	s_barrier
	s_mov_b64 s[68:69], s[28:29]
	ds_read_b128 v[174:177], v145 offset:16384
	ds_read_b128 v[178:181], v145 offset:17408
	ds_read_b128 v[182:185], v145 offset:18432
	ds_read_b128 v[186:189], v145 offset:19456
	ds_read_b128 v[190:193], v145 offset:20480
	ds_read_b128 v[194:197], v145 offset:21504
	ds_read_b128 v[198:201], v145 offset:22528
	ds_read_b128 v[202:205], v145 offset:23552
	s_add_i32 s21, s21, s89
	v_lshl_add_u64 v[132:133], s[68:69], 0, v[112:113]
	s_add_u32 s68, s28, 0x10000
	s_mov_b32 m0, s21
	s_addc_u32 s69, s29, 0
	global_load_lds_dwordx4 v[132:133], off
	s_add_i32 m0, s21, 0x2000
	v_lshl_add_u64 v[132:133], s[68:69], 0, v[112:113]
	s_add_u32 s68, s28, 0x20000
	s_addc_u32 s69, s29, 0
	global_load_lds_dwordx4 v[132:133], off
	s_add_i32 s21, s63, s89
	v_lshl_add_u64 v[132:133], s[68:69], 0, v[112:113]
	s_add_u32 s68, s28, 0x30000
	s_mov_b32 m0, s21
	s_addc_u32 s69, s29, 0
	global_load_lds_dwordx4 v[132:133], off
	s_add_i32 m0, s21, 0x2000
	v_lshl_add_u64 v[132:133], s[68:69], 0, v[112:113]
	s_mov_b64 s[68:69], s[24:25]
	global_load_lds_dwordx4 v[132:133], off
	s_mov_b32 m0, s58
	v_lshl_add_u64 v[132:133], s[68:69], 0, v[130:131]
	s_add_u32 s68, s24, 0x10000
	s_addc_u32 s69, s25, 0
	global_load_lds_dwordx4 v[132:133], off
	s_mov_b32 m0, s73
	v_lshl_add_u64 v[132:133], s[68:69], 0, v[130:131]
	global_load_lds_dwordx4 v[132:133], off
	s_waitcnt vmcnt(8)
	s_waitcnt lgkmcnt(0)
	s_barrier
	s_setprio 1
	s_waitcnt lgkmcnt(0)
	s_cmp_eq_u32 s19, -2
	s_cbranch_scc1 .Lzmu_s1
; #define PG8_STAGE(bufoff, gbase, voff) do { _Pragma("unroll") for (int _i = 0; _i < 2; ++_i) { const char* gb_ = (const char*)(gbase) + _i * rstep; asm volatile("" : "+s"(gb_));   \
;         __builtin_amdgcn_global_load_lds((const unsigned*)(gb_ + (voff)), (LAS unsigned*)(lds + (bufoff) + ldsw + _i * 8192), 16, 0, 0); } } while (0)
; #define PG8_LDA(dst, b, h) do { _Pragma("unroll") for (int m = 0; m < 4; ++m) _Pragma("unroll") for (int k = 0; k < 2; ++k) dst[m][k] = *(const LAS bf16x8*)(lds + PG8_SA(b, h) + aoff + m * 2048 + k * 1024); } while (0)
; #define PG8_LDB(dst, b, h) do { _Pragma("unroll") for (int n = 0; n < 2; ++n) _Pragma("unroll") for (int k = 0; k < 2; ++k) dst[n][k] = *(const LAS bf16x8*)(lds + PG8_SB(b, h) + boff + n * 2048 + k * 1024); } while (0)
; #define PG8_WAIT_V(n) asm volatile("s_waitcnt vmcnt(" #n ")" ::: "memory")
; #define PG8_WAIT_L(n) asm volatile("s_waitcnt lgkmcnt(" #n ")" ::: "memory")
; #define PG8_BAR __builtin_amdgcn_s_barrier()
; #define PG8_SCHED __builtin_amdgcn_sched_barrier(0)
; template <class Epi, class Sched, bool ALIGN_EPI = true, bool SP2 = true, bool I8 = false, bool F8 = false>
; __device__ __forceinline__ void gemm_phase(LAS unsigned char* lds, const int K, const Sched& S, const Epi& E, const int wave) {
;     ...
;             PG8_WAIT_V(8); PG8_WAIT_L(0); PG8_BAR; PG8_MMA(1, 0, At, B0); PG8_MMA(1, 1, At, B1); PG8_BAR; PG8_SCHED;
;             PG8_LDB(B0, 1, 0); PG8_LDB(B1, 1, 1); PG8_SCHED; PG8_LDA(At, 1, 0); PG8_STAGE(PG8_SA(0, 1), a2 + hstep, voffA);
;             PG8_WAIT_V(8); PG8_WAIT_L(0); PG8_BAR; PG8_MMA(0, 0, At, B0); PG8_MMA(0, 1, At, B1); PG8_BAR; PG8_SCHED;
	v_mfma_i32_16x16x64_i8 v[60:63], v[136:139], v[174:177], v[60:63]
	v_mfma_i32_16x16x64_i8 v[52:55], v[146:149], v[174:177], v[52:55]
	v_mfma_i32_16x16x64_i8 v[44:47], v[136:139], v[182:185], v[44:47]
	v_mfma_i32_16x16x64_i8 v[36:39], v[146:149], v[182:185], v[36:39]
	v_mfma_i32_16x16x64_i8 v[28:31], v[136:139], v[190:193], v[28:31]
	v_mfma_i32_16x16x64_i8 v[20:23], v[146:149], v[190:193], v[20:23]
	v_mfma_i32_16x16x64_i8 v[12:15], v[136:139], v[198:201], v[12:15]
	v_mfma_i32_16x16x64_i8 v[4:7], v[146:149], v[198:201], v[4:7]
	v_mfma_i32_16x16x64_i8 v[60:63], v[140:143], v[178:181], v[60:63]
	v_mfma_i32_16x16x64_i8 v[52:55], v[150:153], v[178:181], v[52:55]
	v_mfma_i32_16x16x64_i8 v[44:47], v[140:143], v[186:189], v[44:47]
	v_mfma_i32_16x16x64_i8 v[36:39], v[150:153], v[186:189], v[36:39]
	v_mfma_i32_16x16x64_i8 v[28:31], v[140:143], v[194:197], v[28:31]
	v_mfma_i32_16x16x64_i8 v[20:23], v[150:153], v[194:197], v[20:23]
	v_mfma_i32_16x16x64_i8 v[12:15], v[140:143], v[202:205], v[12:15]
	v_mfma_i32_16x16x64_i8 v[4:7], v[150:153], v[202:205], v[4:7]
	v_mfma_i32_16x16x64_i8 v[56:59], v[154:157], v[174:177], v[56:59]
	v_mfma_i32_16x16x64_i8 v[48:51], v[166:169], v[174:177], v[48:51]
	v_mfma_i32_16x16x64_i8 v[40:43], v[154:157], v[182:185], v[40:43]
	v_mfma_i32_16x16x64_i8 v[32:35], v[166:169], v[182:185], v[32:35]
	v_mfma_i32_16x16x64_i8 v[24:27], v[154:157], v[190:193], v[24:27]
	v_mfma_i32_16x16x64_i8 v[16:19], v[166:169], v[190:193], v[16:19]
	v_mfma_i32_16x16x64_i8 v[8:11], v[154:157], v[198:201], v[8:11]
	v_mfma_i32_16x16x64_i8 v[0:3], v[166:169], v[198:201], v[0:3]
	v_mfma_i32_16x16x64_i8 v[56:59], v[158:161], v[178:181], v[56:59]
	v_mfma_i32_16x16x64_i8 v[48:51], v[170:173], v[178:181], v[48:51]
	v_mfma_i32_16x16x64_i8 v[40:43], v[158:161], v[186:189], v[40:43]
	v_mfma_i32_16x16x64_i8 v[32:35], v[170:173], v[186:189], v[32:35]
	v_mfma_i32_16x16x64_i8 v[24:27], v[158:161], v[194:197], v[24:27]
	v_mfma_i32_16x16x64_i8 v[16:19], v[170:173], v[194:197], v[16:19]
	v_mfma_i32_16x16x64_i8 v[8:11], v[158:161], v[202:205], v[8:11]
	v_mfma_i32_16x16x64_i8 v[0:3], v[170:173], v[202:205], v[0:3]
	s_setprio 0
.Lzmu_r1:
	s_barrier
	s_add_i32 s21, 0, 0x18000
	v_add_u32_e32 v132, s21, v135
	s_add_i32 s63, 0, 0x1c000
	ds_read_b128 v[136:139], v132
	ds_read_b128 v[140:143], v132 offset:1024
	ds_read_b128 v[146:149], v132 offset:2048
	ds_read_b128 v[150:153], v132 offset:3072
	v_add_u32_e32 v132, s63, v135
	ds_read_b128 v[154:157], v132
	ds_read_b128 v[158:161], v132 offset:1024
	ds_read_b128 v[166:169], v132 offset:2048
	ds_read_b128 v[170:173], v132 offset:3072
	s_add_u32 s68, s24, 0x20000
	s_addc_u32 s69, s25, 0
	ds_read_b128 v[174:177], v145 offset:32768
	ds_read_b128 v[178:181], v145 offset:33792
	ds_read_b128 v[182:185], v145 offset:34816
	ds_read_b128 v[186:189], v145 offset:35840
	ds_read_b128 v[190:193], v145 offset:36864
	ds_read_b128 v[194:197], v145 offset:37888
	ds_read_b128 v[198:201], v145 offset:38912
	ds_read_b128 v[202:205], v145 offset:39936
	s_mov_b32 m0, s40
	v_lshl_add_u64 v[132:133], s[68:69], 0, v[130:131]
	s_add_u32 s68, s24, 0x30000
	s_addc_u32 s69, s25, 0
	global_load_lds_dwordx4 v[132:133], off
	s_mov_b32 m0, s41
	v_lshl_add_u64 v[132:133], s[68:69], 0, v[130:131]
	global_load_lds_dwordx4 v[132:133], off
	s_waitcnt vmcnt(8)
	s_waitcnt lgkmcnt(0)
	s_barrier
	s_setprio 1
	s_waitcnt lgkmcnt(0)
	v_mfma_i32_16x16x64_i8 v[126:129], v[136:139], v[174:177], v[126:129]
	v_mfma_i32_16x16x64_i8 v[118:121], v[146:149], v[174:177], v[118:121]
	v_mfma_i32_16x16x64_i8 v[108:111], v[136:139], v[182:185], v[108:111]
	v_mfma_i32_16x16x64_i8 v[100:103], v[146:149], v[182:185], v[100:103]
	v_mfma_i32_16x16x64_i8 v[92:95], v[136:139], v[190:193], v[92:95]
	v_mfma_i32_16x16x64_i8 v[84:87], v[146:149], v[190:193], v[84:87]
	v_mfma_i32_16x16x64_i8 v[76:79], v[136:139], v[198:201], v[76:79]
	v_mfma_i32_16x16x64_i8 v[68:71], v[146:149], v[198:201], v[68:71]
	v_mfma_i32_16x16x64_i8 v[126:129], v[140:143], v[178:181], v[126:129]
	v_mfma_i32_16x16x64_i8 v[118:121], v[150:153], v[178:181], v[118:121]
	v_mfma_i32_16x16x64_i8 v[108:111], v[140:143], v[186:189], v[108:111]
	v_mfma_i32_16x16x64_i8 v[100:103], v[150:153], v[186:189], v[100:103]
	v_mfma_i32_16x16x64_i8 v[92:95], v[140:143], v[194:197], v[92:95]
	v_mfma_i32_16x16x64_i8 v[84:87], v[150:153], v[194:197], v[84:87]
	v_mfma_i32_16x16x64_i8 v[76:79], v[140:143], v[202:205], v[76:79]
	v_mfma_i32_16x16x64_i8 v[68:71], v[150:153], v[202:205], v[68:71]
	v_mfma_i32_16x16x64_i8 v[122:125], v[154:157], v[174:177], v[122:125]
	v_mfma_i32_16x16x64_i8 v[114:117], v[166:169], v[174:177], v[114:117]
	v_mfma_i32_16x16x64_i8 v[104:107], v[154:157], v[182:185], v[104:107]
	v_mfma_i32_16x16x64_i8 v[96:99], v[166:169], v[182:185], v[96:99]
	v_mfma_i32_16x16x64_i8 v[88:91], v[154:157], v[190:193], v[88:91]
	v_mfma_i32_16x16x64_i8 v[80:83], v[166:169], v[190:193], v[80:83]
	v_mfma_i32_16x16x64_i8 v[72:75], v[154:157], v[198:201], v[72:75]
	v_mfma_i32_16x16x64_i8 v[64:67], v[166:169], v[198:201], v[64:67]
	v_mfma_i32_16x16x64_i8 v[122:125], v[158:161], v[178:181], v[122:125]
	v_mfma_i32_16x16x64_i8 v[114:117], v[170:173], v[178:181], v[114:117]
	v_mfma_i32_16x16x64_i8 v[104:107], v[158:161], v[186:189], v[104:107]
	v_mfma_i32_16x16x64_i8 v[96:99], v[170:173], v[186:189], v[96:99]
	v_mfma_i32_16x16x64_i8 v[88:91], v[158:161], v[194:197], v[88:91]
	v_mfma_i32_16x16x64_i8 v[80:83], v[170:173], v[194:197], v[80:83]
	v_mfma_i32_16x16x64_i8 v[72:75], v[158:161], v[202:205], v[72:75]
	v_mfma_i32_16x16x64_i8 v[64:67], v[170:173], v[202:205], v[64:67]
	s_setprio 0
	s_barrier
; #define PG8_STAGE(bufoff, gbase, voff) do { _Pragma("unroll") for (int _i = 0; _i < 2; ++_i) { const char* gb_ = (const char*)(gbase) + _i * rstep; asm volatile("" : "+s"(gb_));   \
;         __builtin_amdgcn_global_load_lds((const unsigned*)(gb_ + (voff)), (LAS unsigned*)(lds + (bufoff) + ldsw + _i * 8192), 16, 0, 0); } } while (0)
; #define PG8_LDA(dst, b, h) do { _Pragma("unroll") for (int m = 0; m < 4; ++m) _Pragma("unroll") for (int k = 0; k < 2; ++k) dst[m][k] = *(const LAS bf16x8*)(lds + PG8_SA(b, h) + aoff + m * 2048 + k * 1024); } while (0)
; #define PG8_WAIT_V(n) asm volatile("s_waitcnt vmcnt(" #n ")" ::: "memory")
; #define PG8_WAIT_L(n) asm volatile("s_waitcnt lgkmcnt(" #n ")" ::: "memory")
; #define PG8_BAR __builtin_amdgcn_s_barrier()
; #define PG8_SCHED __builtin_amdgcn_sched_barrier(0)
; template <class Epi, class Sched, bool ALIGN_EPI = true, bool SP2 = true, bool I8 = false, bool F8 = false>
; __device__ __forceinline__ void gemm_phase(LAS unsigned char* lds, const int K, const Sched& S, const Epi& E, const int wave) {
;     ...
;             PG8_WAIT_V(8); PG8_WAIT_L(0); PG8_BAR; PG8_MMA(0, 0, At, B0); PG8_MMA(0, 1, At, B1); PG8_BAR; PG8_SCHED;
;             PG8_LDA(At, 1, 1); PG8_STAGE(PG8_SB(1, 0), b3, voffB); PG8_STAGE(PG8_SB(1, 1), b3 + hstep, voffB); PG8_STAGE(PG8_SA(1, 0), a3, voffA);
;             PG8_WAIT_V(8); PG8_WAIT_L(0); PG8_BAR; PG8_MMA(1, 0, At, B0); PG8_MMA(1, 1, At, B1); PG8_BAR; PG8_SCHED;
	s_add_u32 s68, s28, 0x80
	s_addc_u32 s69, s29, 0
	ds_read_b128 v[174:177], v145 offset:49152
	ds_read_b128 v[178:181], v145 offset:50176
	ds_read_b128 v[182:185], v145 offset:51200
	ds_read_b128 v[186:189], v145 offset:52224
	ds_read_b128 v[190:193], v145 offset:53248
	ds_read_b128 v[194:197], v145 offset:54272
	ds_read_b128 v[198:201], v145 offset:55296
	ds_read_b128 v[202:205], v145 offset:56320
	s_add_i32 s21, s21, s89
	v_lshl_add_u64 v[132:133], s[68:69], 0, v[112:113]
	s_add_u32 s68, s28, 0x10080
	s_mov_b32 m0, s21
	s_addc_u32 s69, s29, 0
	global_load_lds_dwordx4 v[132:133], off
	s_add_i32 m0, s21, 0x2000
	v_lshl_add_u64 v[132:133], s[68:69], 0, v[112:113]
	s_add_u32 s68, s28, 0x20080
	s_addc_u32 s69, s29, 0
	s_add_i32 s21, s63, s89
	global_load_lds_dwordx4 v[132:133], off
	s_mov_b32 m0, s21
	v_lshl_add_u64 v[132:133], s[68:69], 0, v[112:113]
	s_add_u32 s28, s28, 0x30080
	global_load_lds_dwordx4 v[132:133], off
	s_addc_u32 s29, s29, 0
	s_add_i32 m0, s21, 0x2000
	s_add_u32 s24, s24, 0x10080
	v_lshl_add_u64 v[132:133], s[28:29], 0, v[112:113]
	global_load_lds_dwordx4 v[132:133], off
	s_mov_b32 m0, s59
	v_lshl_add_u64 v[132:133], s[26:27], 0, v[130:131]
	s_addc_u32 s25, s25, 0
	global_load_lds_dwordx4 v[132:133], off
	s_mov_b32 m0, s81
	v_lshl_add_u64 v[132:133], s[24:25], 0, v[130:131]
	global_load_lds_dwordx4 v[132:133], off
	s_waitcnt vmcnt(8)
	s_waitcnt lgkmcnt(0)
	s_barrier
	s_setprio 1
	s_waitcnt lgkmcnt(0)
	v_mfma_i32_16x16x64_i8 v[60:63], v[136:139], v[174:177], v[60:63]
	v_mfma_i32_16x16x64_i8 v[52:55], v[146:149], v[174:177], v[52:55]
	v_mfma_i32_16x16x64_i8 v[44:47], v[136:139], v[182:185], v[44:47]
	v_mfma_i32_16x16x64_i8 v[36:39], v[146:149], v[182:185], v[36:39]
	v_mfma_i32_16x16x64_i8 v[28:31], v[136:139], v[190:193], v[28:31]
	v_mfma_i32_16x16x64_i8 v[20:23], v[146:149], v[190:193], v[20:23]
	v_mfma_i32_16x16x64_i8 v[12:15], v[136:139], v[198:201], v[12:15]
	v_mfma_i32_16x16x64_i8 v[4:7], v[146:149], v[198:201], v[4:7]
	v_mfma_i32_16x16x64_i8 v[60:63], v[140:143], v[178:181], v[60:63]
	v_mfma_i32_16x16x64_i8 v[52:55], v[150:153], v[178:181], v[52:55]
	v_mfma_i32_16x16x64_i8 v[44:47], v[140:143], v[186:189], v[44:47]
	v_mfma_i32_16x16x64_i8 v[36:39], v[150:153], v[186:189], v[36:39]
	v_mfma_i32_16x16x64_i8 v[28:31], v[140:143], v[194:197], v[28:31]
	v_mfma_i32_16x16x64_i8 v[20:23], v[150:153], v[194:197], v[20:23]
	v_mfma_i32_16x16x64_i8 v[12:15], v[140:143], v[202:205], v[12:15]
	v_mfma_i32_16x16x64_i8 v[4:7], v[150:153], v[202:205], v[4:7]
	v_mfma_i32_16x16x64_i8 v[56:59], v[154:157], v[174:177], v[56:59]
	v_mfma_i32_16x16x64_i8 v[48:51], v[166:169], v[174:177], v[48:51]
	v_mfma_i32_16x16x64_i8 v[40:43], v[154:157], v[182:185], v[40:43]
	v_mfma_i32_16x16x64_i8 v[32:35], v[166:169], v[182:185], v[32:35]
	v_mfma_i32_16x16x64_i8 v[24:27], v[154:157], v[190:193], v[24:27]
	v_mfma_i32_16x16x64_i8 v[16:19], v[166:169], v[190:193], v[16:19]
	v_mfma_i32_16x16x64_i8 v[8:11], v[154:157], v[198:201], v[8:11]
	v_mfma_i32_16x16x64_i8 v[0:3], v[166:169], v[198:201], v[0:3]
	v_mfma_i32_16x16x64_i8 v[56:59], v[158:161], v[178:181], v[56:59]
	v_mfma_i32_16x16x64_i8 v[48:51], v[170:173], v[178:181], v[48:51]
	v_mfma_i32_16x16x64_i8 v[40:43], v[158:161], v[186:189], v[40:43]
	v_mfma_i32_16x16x64_i8 v[32:35], v[170:173], v[186:189], v[32:35]
	v_mfma_i32_16x16x64_i8 v[24:27], v[158:161], v[194:197], v[24:27]
	v_mfma_i32_16x16x64_i8 v[16:19], v[170:173], v[194:197], v[16:19]
	v_mfma_i32_16x16x64_i8 v[8:11], v[158:161], v[202:205], v[8:11]
	v_mfma_i32_16x16x64_i8 v[0:3], v[170:173], v[202:205], v[0:3]
	s_setprio 0
	s_barrier
	s_add_i32 s19, s19, 2
	s_add_u32 s11, s11, 0x100
	s_addc_u32 s13, s13, 0
	s_add_u32 s22, s22, 0x100
	s_addc_u32 s23, s23, 0
	s_cmp_gt_u32 s19, 5
	s_cbranch_scc0 .LBB0_1540
	s_and_b64 vcc, exec, s[8:9]
	s_cbranch_vccz .LBB0_1543
	s_barrier

; #define PG8_STAGE(bufoff, gbase, voff) do { _Pragma("unroll") for (int _i = 0; _i < 2; ++_i) { const char* gb_ = (const char*)(gbase) + _i * rstep; asm volatile("" : "+s"(gb_));   \
;         __builtin_amdgcn_global_load_lds((const unsigned*)(gb_ + (voff)), (LAS unsigned*)(lds + (bufoff) + ldsw + _i * 8192), 16, 0, 0); } } while (0)
; #define PG8_LDA(dst, b, h) do { _Pragma("unroll") for (int m = 0; m < 4; ++m) _Pragma("unroll") for (int k = 0; k < 2; ++k) dst[m][k] = *(const LAS bf16x8*)(lds + PG8_SA(b, h) + aoff + m * 2048 + k * 1024); } while (0)
; #define PG8_LDB(dst, b, h) do { _Pragma("unroll") for (int n = 0; n < 2; ++n) _Pragma("unroll") for (int k = 0; k < 2; ++k) dst[n][k] = *(const LAS bf16x8*)(lds + PG8_SB(b, h) + boff + n * 2048 + k * 1024); } while (0)
; #define PG8_WAIT_V(n) asm volatile("s_waitcnt vmcnt(" #n ")" ::: "memory")
; #define PG8_WAIT_L(n) asm volatile("s_waitcnt lgkmcnt(" #n ")" ::: "memory")
; #define PG8_BAR __builtin_amdgcn_s_barrier()
; #define PG8_SCHED __builtin_amdgcn_sched_barrier(0)
; template <class Epi, class Sched, bool ALIGN_EPI = true, bool SP2 = true, bool I8 = false, bool F8 = false>
; __device__ __forceinline__ void gemm_phase(LAS unsigned char* lds, const int K, const Sched& S, const Epi& E, const int wave) {
;     ...
;         const char* nA = has_next ? nxt.a : cA; const char* nB = has_next ? nxt.b : cB;
;         for (int t = 0; t < nt; t += 2) {
;             const bool last = (t == nt - 2);
;             const char* a1 = cA + (size_t)(t + 1) * kstep;
;             const char* a2 = last ? nA : cA + (size_t)(t + 2) * kstep; const char* b2 = last ? nB : cB + (size_t)(t + 2) * kstep;
;             const char* a3 = a2 + kstep; const char* b3 = b2 + kstep;
;             if constexpr (SP2) {
;             PG8_LDB(B0, 0, 0); PG8_LDB(B1, 0, 1); PG8_SCHED; PG8_LDA(At, 0, 0); PG8_STAGE(PG8_SA(1, 1), a1 + hstep, voffA);
;             PG8_WAIT_V(8); PG8_WAIT_L(0); PG8_BAR; PG8_MMA(0, 0, At, B0); PG8_MMA(0, 1, At, B1); PG8_BAR; PG8_SCHED;
;             PG8_LDA(At, 0, 1); PG8_STAGE(PG8_SB(0, 0), b2, voffB); PG8_STAGE(PG8_SB(0, 1), b2 + hstep, voffB); PG8_STAGE(PG8_SA(0, 0), a2, voffA);
;             PG8_WAIT_V(8); PG8_WAIT_L(0); PG8_BAR; PG8_MMA(1, 0, At, B0); PG8_MMA(1, 1, At, B1); PG8_BAR; PG8_SCHED;
.LBB0_1767:
	s_add_u32 s20, s18, 0xfffd0080
	s_addc_u32 s21, s19, -1
	s_cmp_eq_u32 s46, 4
	s_cselect_b32 s20, s12, s20
	s_cselect_b32 s21, s13, s21
	s_cselect_b32 s24, s14, s9
	s_cselect_b32 s25, s15, s11
	s_add_u32 s22, s20, 0x80
	s_addc_u32 s23, s21, 0
	s_add_i32 s47, 0, 0x10000
	v_add_u32_e32 v136, s47, v137
	s_add_i32 s50, 0, 0x14000
	ds_read_b128 v[132:135], v136
	ds_read_b128 v[138:141], v136 offset:1024
	ds_read_b128 v[142:145], v136 offset:2048
	ds_read_b128 v[150:153], v136 offset:3072
	v_add_u32_e32 v136, s50, v137
	ds_read_b128 v[154:157], v136
	ds_read_b128 v[158:161], v136 offset:1024
	ds_read_b128 v[166:169], v136 offset:2048
	ds_read_b128 v[170:173], v136 offset:3072
	s_add_u32 s48, s18, 0xffff0000
	s_addc_u32 s49, s19, -1
	ds_read_b128 v[174:177], v149
	ds_read_b128 v[178:181], v149 offset:1024
	ds_read_b128 v[182:185], v149 offset:2048
	ds_read_b128 v[186:189], v149 offset:3072
	ds_read_b128 v[190:193], v149 offset:4096
	ds_read_b128 v[194:197], v149 offset:5120
	ds_read_b128 v[198:201], v149 offset:6144
	ds_read_b128 v[202:205], v149 offset:7168
	s_add_i32 m0, s38, 0xc000
	v_lshl_add_u64 v[146:147], s[48:49], 0, v[130:131]
	s_mov_b64 s[48:49], s[18:19]
	global_load_lds_dwordx4 v[146:147], off
	s_add_i32 m0, s38, 0xe000
	v_lshl_add_u64 v[146:147], s[48:49], 0, v[130:131]
	global_load_lds_dwordx4 v[146:147], off
	s_waitcnt vmcnt(8)
	s_waitcnt lgkmcnt(0)
	s_barrier
	s_setprio 1
	s_waitcnt lgkmcnt(0)
	s_cmp_eq_u32 s46, -2
	s_cbranch_scc1 .Lzdu_s0
	v_mfma_i32_16x16x64_i8 v[126:129], v[132:135], v[174:177], v[126:129]
	v_mfma_i32_16x16x64_i8 v[118:121], v[142:145], v[174:177], v[118:121]
	v_mfma_i32_16x16x64_i8 v[108:111], v[132:135], v[182:185], v[108:111]
	v_mfma_i32_16x16x64_i8 v[100:103], v[142:145], v[182:185], v[100:103]
	v_mfma_i32_16x16x64_i8 v[92:95], v[132:135], v[190:193], v[92:95]
	v_mfma_i32_16x16x64_i8 v[84:87], v[142:145], v[190:193], v[84:87]
	v_mfma_i32_16x16x64_i8 v[76:79], v[132:135], v[198:201], v[76:79]
	v_mfma_i32_16x16x64_i8 v[68:71], v[142:145], v[198:201], v[68:71]
	v_mfma_i32_16x16x64_i8 v[126:129], v[138:141], v[178:181], v[126:129]
	v_mfma_i32_16x16x64_i8 v[118:121], v[150:153], v[178:181], v[118:121]
	v_mfma_i32_16x16x64_i8 v[108:111], v[138:141], v[186:189], v[108:111]
	v_mfma_i32_16x16x64_i8 v[100:103], v[150:153], v[186:189], v[100:103]
	v_mfma_i32_16x16x64_i8 v[92:95], v[138:141], v[194:197], v[92:95]
	v_mfma_i32_16x16x64_i8 v[84:87], v[150:153], v[194:197], v[84:87]
	v_mfma_i32_16x16x64_i8 v[76:79], v[138:141], v[202:205], v[76:79]
	v_mfma_i32_16x16x64_i8 v[68:71], v[150:153], v[202:205], v[68:71]
	v_mfma_i32_16x16x64_i8 v[122:125], v[154:157], v[174:177], v[122:125]
	v_mfma_i32_16x16x64_i8 v[114:117], v[166:169], v[174:177], v[114:117]
	v_mfma_i32_16x16x64_i8 v[104:107], v[154:157], v[182:185], v[104:107]
	v_mfma_i32_16x16x64_i8 v[96:99], v[166:169], v[182:185], v[96:99]
	v_mfma_i32_16x16x64_i8 v[88:91], v[154:157], v[190:193], v[88:91]
	v_mfma_i32_16x16x64_i8 v[80:83], v[166:169], v[190:193], v[80:83]
	v_mfma_i32_16x16x64_i8 v[72:75], v[154:157], v[198:201], v[72:75]
	v_mfma_i32_16x16x64_i8 v[64:67], v[166:169], v[198:201], v[64:67]
	v_mfma_i32_16x16x64_i8 v[122:125], v[158:161], v[178:181], v[122:125]
	v_mfma_i32_16x16x64_i8 v[114:117], v[170:173], v[178:181], v[114:117]
	v_mfma_i32_16x16x64_i8 v[104:107], v[158:161], v[186:189], v[104:107]
	v_mfma_i32_16x16x64_i8 v[96:99], v[170:173], v[186:189], v[96:99]
	v_mfma_i32_16x16x64_i8 v[88:91], v[158:161], v[194:197], v[88:91]
	v_mfma_i32_16x16x64_i8 v[80:83], v[170:173], v[194:197], v[80:83]
	v_mfma_i32_16x16x64_i8 v[72:75], v[158:161], v[202:205], v[72:75]
	v_mfma_i32_16x16x64_i8 v[64:67], v[170:173], v[202:205], v[64:67]
	s_setprio 0
.Lzdu_r0:
	s_barrier
	s_mov_b64 s[48:49], s[24:25]
	ds_read_b128 v[174:177], v149 offset:16384
	ds_read_b128 v[178:181], v149 offset:17408
	ds_read_b128 v[182:185], v149 offset:18432
	ds_read_b128 v[186:189], v149 offset:19456
	ds_read_b128 v[190:193], v149 offset:20480
	ds_read_b128 v[194:197], v149 offset:21504
	ds_read_b128 v[198:201], v149 offset:22528
	ds_read_b128 v[202:205], v149 offset:23552
	s_add_i32 s47, s47, s28
	v_lshl_add_u64 v[146:147], s[48:49], 0, v[112:113]
	s_add_u32 s48, s24, 0x10000
	s_mov_b32 m0, s47
	s_addc_u32 s49, s25, 0
	global_load_lds_dwordx4 v[146:147], off
	s_add_i32 m0, s47, 0x2000
	v_lshl_add_u64 v[146:147], s[48:49], 0, v[112:113]
	s_add_u32 s48, s24, 0x20000
	s_addc_u32 s49, s25, 0
	global_load_lds_dwordx4 v[146:147], off
	s_add_i32 s47, s50, s28
	v_lshl_add_u64 v[146:147], s[48:49], 0, v[112:113]
	s_add_u32 s48, s24, 0x30000
	s_mov_b32 m0, s47
	s_addc_u32 s49, s25, 0
	global_load_lds_dwordx4 v[146:147], off
	s_add_i32 m0, s47, 0x2000
	v_lshl_add_u64 v[146:147], s[48:49], 0, v[112:113]
	s_mov_b64 s[48:49], s[20:21]
	global_load_lds_dwordx4 v[146:147], off
	s_mov_b32 m0, s38
	v_lshl_add_u64 v[146:147], s[48:49], 0, v[130:131]
	s_add_u32 s48, s20, 0x10000
	s_addc_u32 s49, s21, 0
	global_load_lds_dwordx4 v[146:147], off
	s_mov_b32 m0, s39
	v_lshl_add_u64 v[146:147], s[48:49], 0, v[130:131]
	global_load_lds_dwordx4 v[146:147], off
	s_waitcnt vmcnt(8)
	s_waitcnt lgkmcnt(0)
	s_barrier
	s_setprio 1
	s_waitcnt lgkmcnt(0)
	s_cmp_eq_u32 s46, -2
	s_cbranch_scc1 .Lzdu_s1
; #define PG8_STAGE(bufoff, gbase, voff) do { _Pragma("unroll") for (int _i = 0; _i < 2; ++_i) { const char* gb_ = (const char*)(gbase) + _i * rstep; asm volatile("" : "+s"(gb_));   \
;         __builtin_amdgcn_global_load_lds((const unsigned*)(gb_ + (voff)), (LAS unsigned*)(lds + (bufoff) + ldsw + _i * 8192), 16, 0, 0); } } while (0)
; #define PG8_LDA(dst, b, h) do { _Pragma("unroll") for (int m = 0; m < 4; ++m) _Pragma("unroll") for (int k = 0; k < 2; ++k) dst[m][k] = *(const LAS bf16x8*)(lds + PG8_SA(b, h) + aoff + m * 2048 + k * 1024); } while (0)
; #define PG8_LDB(dst, b, h) do { _Pragma("unroll") for (int n = 0; n < 2; ++n) _Pragma("unroll") for (int k = 0; k < 2; ++k) dst[n][k] = *(const LAS bf16x8*)(lds + PG8_SB(b, h) + boff + n * 2048 + k * 1024); } while (0)
; #define PG8_WAIT_V(n) asm volatile("s_waitcnt vmcnt(" #n ")" ::: "memory")
; #define PG8_WAIT_L(n) asm volatile("s_waitcnt lgkmcnt(" #n ")" ::: "memory")
; #define PG8_BAR __builtin_amdgcn_s_barrier()
; #define PG8_SCHED __builtin_amdgcn_sched_barrier(0)
; template <class Epi, class Sched, bool ALIGN_EPI = true, bool SP2 = true, bool I8 = false, bool F8 = false>
; __device__ __forceinline__ void gemm_phase(LAS unsigned char* lds, const int K, const Sched& S, const Epi& E, const int wave) {
;     ...
;             PG8_WAIT_V(8); PG8_WAIT_L(0); PG8_BAR; PG8_MMA(1, 0, At, B0); PG8_MMA(1, 1, At, B1); PG8_BAR; PG8_SCHED;
;             PG8_LDB(B0, 1, 0); PG8_LDB(B1, 1, 1); PG8_SCHED; PG8_LDA(At, 1, 0); PG8_STAGE(PG8_SA(0, 1), a2 + hstep, voffA);
;             PG8_WAIT_V(8); PG8_WAIT_L(0); PG8_BAR; PG8_MMA(0, 0, At, B0); PG8_MMA(0, 1, At, B1); PG8_BAR; PG8_SCHED;
	v_mfma_i32_16x16x64_i8 v[60:63], v[132:135], v[174:177], v[60:63]
	v_mfma_i32_16x16x64_i8 v[52:55], v[142:145], v[174:177], v[52:55]
	v_mfma_i32_16x16x64_i8 v[44:47], v[132:135], v[182:185], v[44:47]
	v_mfma_i32_16x16x64_i8 v[36:39], v[142:145], v[182:185], v[36:39]
	v_mfma_i32_16x16x64_i8 v[28:31], v[132:135], v[190:193], v[28:31]
	v_mfma_i32_16x16x64_i8 v[20:23], v[142:145], v[190:193], v[20:23]
	v_mfma_i32_16x16x64_i8 v[12:15], v[132:135], v[198:201], v[12:15]
	v_mfma_i32_16x16x64_i8 v[4:7], v[142:145], v[198:201], v[4:7]
	v_mfma_i32_16x16x64_i8 v[60:63], v[138:141], v[178:181], v[60:63]
	v_mfma_i32_16x16x64_i8 v[52:55], v[150:153], v[178:181], v[52:55]
	v_mfma_i32_16x16x64_i8 v[44:47], v[138:141], v[186:189], v[44:47]
	v_mfma_i32_16x16x64_i8 v[36:39], v[150:153], v[186:189], v[36:39]
	v_mfma_i32_16x16x64_i8 v[28:31], v[138:141], v[194:197], v[28:31]
	v_mfma_i32_16x16x64_i8 v[20:23], v[150:153], v[194:197], v[20:23]
	v_mfma_i32_16x16x64_i8 v[12:15], v[138:141], v[202:205], v[12:15]
	v_mfma_i32_16x16x64_i8 v[4:7], v[150:153], v[202:205], v[4:7]
	v_mfma_i32_16x16x64_i8 v[56:59], v[154:157], v[174:177], v[56:59]
	v_mfma_i32_16x16x64_i8 v[48:51], v[166:169], v[174:177], v[48:51]
	v_mfma_i32_16x16x64_i8 v[40:43], v[154:157], v[182:185], v[40:43]
	v_mfma_i32_16x16x64_i8 v[32:35], v[166:169], v[182:185], v[32:35]
	v_mfma_i32_16x16x64_i8 v[24:27], v[154:157], v[190:193], v[24:27]
	v_mfma_i32_16x16x64_i8 v[16:19], v[166:169], v[190:193], v[16:19]
	v_mfma_i32_16x16x64_i8 v[8:11], v[154:157], v[198:201], v[8:11]
	v_mfma_i32_16x16x64_i8 v[0:3], v[166:169], v[198:201], v[0:3]
	v_mfma_i32_16x16x64_i8 v[56:59], v[158:161], v[178:181], v[56:59]
	v_mfma_i32_16x16x64_i8 v[48:51], v[170:173], v[178:181], v[48:51]
	v_mfma_i32_16x16x64_i8 v[40:43], v[158:161], v[186:189], v[40:43]
	v_mfma_i32_16x16x64_i8 v[32:35], v[170:173], v[186:189], v[32:35]
	v_mfma_i32_16x16x64_i8 v[24:27], v[158:161], v[194:197], v[24:27]
	v_mfma_i32_16x16x64_i8 v[16:19], v[170:173], v[194:197], v[16:19]
	v_mfma_i32_16x16x64_i8 v[8:11], v[158:161], v[202:205], v[8:11]
	v_mfma_i32_16x16x64_i8 v[0:3], v[170:173], v[202:205], v[0:3]
	s_setprio 0
.Lzdu_r1:
	s_barrier
	s_add_i32 s47, 0, 0x18000
	v_add_u32_e32 v136, s47, v137
	s_add_i32 s50, 0, 0x1c000
	ds_read_b128 v[132:135], v136
	ds_read_b128 v[138:141], v136 offset:1024
	ds_read_b128 v[142:145], v136 offset:2048
	ds_read_b128 v[150:153], v136 offset:3072
	v_add_u32_e32 v136, s50, v137
	ds_read_b128 v[154:157], v136
	ds_read_b128 v[158:161], v136 offset:1024
	ds_read_b128 v[166:169], v136 offset:2048
	ds_read_b128 v[170:173], v136 offset:3072
	s_add_u32 s48, s20, 0x20000
	s_addc_u32 s49, s21, 0
	ds_read_b128 v[174:177], v149 offset:32768
	ds_read_b128 v[178:181], v149 offset:33792
	ds_read_b128 v[182:185], v149 offset:34816
	ds_read_b128 v[186:189], v149 offset:35840
	ds_read_b128 v[190:193], v149 offset:36864
	ds_read_b128 v[194:197], v149 offset:37888
	ds_read_b128 v[198:201], v149 offset:38912
	ds_read_b128 v[202:205], v149 offset:39936
	s_mov_b32 m0, s40
	v_lshl_add_u64 v[146:147], s[48:49], 0, v[130:131]
	s_add_u32 s48, s20, 0x30000
	s_addc_u32 s49, s21, 0
	global_load_lds_dwordx4 v[146:147], off
	s_mov_b32 m0, s41
	v_lshl_add_u64 v[146:147], s[48:49], 0, v[130:131]
	global_load_lds_dwordx4 v[146:147], off
	s_waitcnt vmcnt(8)
	s_waitcnt lgkmcnt(0)
	s_barrier
	s_setprio 1
	s_waitcnt lgkmcnt(0)
	v_mfma_i32_16x16x64_i8 v[126:129], v[132:135], v[174:177], v[126:129]
	v_mfma_i32_16x16x64_i8 v[118:121], v[142:145], v[174:177], v[118:121]
	v_mfma_i32_16x16x64_i8 v[108:111], v[132:135], v[182:185], v[108:111]
	v_mfma_i32_16x16x64_i8 v[100:103], v[142:145], v[182:185], v[100:103]
	v_mfma_i32_16x16x64_i8 v[92:95], v[132:135], v[190:193], v[92:95]
	v_mfma_i32_16x16x64_i8 v[84:87], v[142:145], v[190:193], v[84:87]
	v_mfma_i32_16x16x64_i8 v[76:79], v[132:135], v[198:201], v[76:79]
	v_mfma_i32_16x16x64_i8 v[68:71], v[142:145], v[198:201], v[68:71]
	v_mfma_i32_16x16x64_i8 v[126:129], v[138:141], v[178:181], v[126:129]
	v_mfma_i32_16x16x64_i8 v[118:121], v[150:153], v[178:181], v[118:121]
	v_mfma_i32_16x16x64_i8 v[108:111], v[138:141], v[186:189], v[108:111]
	v_mfma_i32_16x16x64_i8 v[100:103], v[150:153], v[186:189], v[100:103]
	v_mfma_i32_16x16x64_i8 v[92:95], v[138:141], v[194:197], v[92:95]
	v_mfma_i32_16x16x64_i8 v[84:87], v[150:153], v[194:197], v[84:87]
	v_mfma_i32_16x16x64_i8 v[76:79], v[138:141], v[202:205], v[76:79]
	v_mfma_i32_16x16x64_i8 v[68:71], v[150:153], v[202:205], v[68:71]
	v_mfma_i32_16x16x64_i8 v[122:125], v[154:157], v[174:177], v[122:125]
	v_mfma_i32_16x16x64_i8 v[114:117], v[166:169], v[174:177], v[114:117]
	v_mfma_i32_16x16x64_i8 v[104:107], v[154:157], v[182:185], v[104:107]
	v_mfma_i32_16x16x64_i8 v[96:99], v[166:169], v[182:185], v[96:99]
	v_mfma_i32_16x16x64_i8 v[88:91], v[154:157], v[190:193], v[88:91]
	v_mfma_i32_16x16x64_i8 v[80:83], v[166:169], v[190:193], v[80:83]
	v_mfma_i32_16x16x64_i8 v[72:75], v[154:157], v[198:201], v[72:75]
	v_mfma_i32_16x16x64_i8 v[64:67], v[166:169], v[198:201], v[64:67]
	v_mfma_i32_16x16x64_i8 v[122:125], v[158:161], v[178:181], v[122:125]
	v_mfma_i32_16x16x64_i8 v[114:117], v[170:173], v[178:181], v[114:117]
	v_mfma_i32_16x16x64_i8 v[104:107], v[158:161], v[186:189], v[104:107]
	v_mfma_i32_16x16x64_i8 v[96:99], v[170:173], v[186:189], v[96:99]
	v_mfma_i32_16x16x64_i8 v[88:91], v[158:161], v[194:197], v[88:91]
	v_mfma_i32_16x16x64_i8 v[80:83], v[170:173], v[194:197], v[80:83]
	v_mfma_i32_16x16x64_i8 v[72:75], v[158:161], v[202:205], v[72:75]
	v_mfma_i32_16x16x64_i8 v[64:67], v[170:173], v[202:205], v[64:67]
	s_setprio 0
	s_barrier
; #define PG8_STAGE(bufoff, gbase, voff) do { _Pragma("unroll") for (int _i = 0; _i < 2; ++_i) { const char* gb_ = (const char*)(gbase) + _i * rstep; asm volatile("" : "+s"(gb_));   \
;         __builtin_amdgcn_global_load_lds((const unsigned*)(gb_ + (voff)), (LAS unsigned*)(lds + (bufoff) + ldsw + _i * 8192), 16, 0, 0); } } while (0)
; #define PG8_WAIT_V(n) asm volatile("s_waitcnt vmcnt(" #n ")" ::: "memory")
; #define PG8_WAIT_L(n) asm volatile("s_waitcnt lgkmcnt(" #n ")" ::: "memory")
; #define PG8_BAR __builtin_amdgcn_s_barrier()
; template <class Epi, class Sched, bool ALIGN_EPI = true, bool SP2 = true, bool I8 = false, bool F8 = false>
; __device__ __forceinline__ void gemm_phase(LAS unsigned char* lds, const int K, const Sched& S, const Epi& E, const int wave) {
;     ...
;             PG8_LDA(At, 1, 1); PG8_STAGE(PG8_SB(1, 0), b3, voffB); PG8_STAGE(PG8_SB(1, 1), b3 + hstep, voffB); PG8_STAGE(PG8_SA(1, 0), a3, voffA);
;             PG8_WAIT_V(8); PG8_WAIT_L(0); PG8_BAR; PG8_MMA(1, 0, At, B0); PG8_MMA(1, 1, At, B1); PG8_BAR; PG8_SCHED;
;             } else {
;             PG8_LDB(B0, 0, 0); PG8_SCHED; PG8_LDA(At, 0, 0); PG8_STAGE(PG8_SA(1, 1), a1 + hstep, voffA);
;             PG8_WAIT_L(8); PG8_BAR; PG8_WAIT_L(0); PG8_MMA(0, 0, At, B0); PG8_BAR; PG8_SCHED;
;             PG8_LDB(B1, 0, 1); PG8_STAGE(PG8_SB(0, 0), b2, voffB);
;             PG8_BAR; PG8_WAIT_L(0); PG8_MMA(0, 1, At, B1); PG8_BAR;
;             PG8_LDA(At, 0, 1); PG8_STAGE(PG8_SA(0, 0), a2, voffA);
;             PG8_BAR; PG8_WAIT_L(0); PG8_MMA(1, 0, At, B0); PG8_BAR; PG8_SCHED;
;             PG8_STAGE(PG8_SB(0, 1), b2 + hstep, voffB);
;             PG8_WAIT_V(6); PG8_BAR; PG8_MMA(1, 1, At, B1); PG8_BAR;
;             PG8_LDB(B0, 1, 0); PG8_SCHED; PG8_LDA(At, 1, 0); PG8_STAGE(PG8_SA(0, 1), a2 + hstep, voffA);
;             PG8_WAIT_L(8); PG8_BAR; PG8_WAIT_L(0); PG8_MMA(0, 0, At, B0); PG8_BAR; PG8_SCHED;
;             PG8_LDB(B1, 1, 1); PG8_STAGE(PG8_SB(1, 0), b3, voffB);
;             PG8_BAR; PG8_WAIT_L(0); PG8_MMA(0, 1, At, B1); PG8_BAR;
;             PG8_LDA(At, 1, 1); PG8_STAGE(PG8_SA(1, 0), a3, voffA);
;             PG8_BAR; PG8_WAIT_L(0); PG8_MMA(1, 0, At, B0); PG8_BAR; PG8_SCHED;
;             PG8_STAGE(PG8_SB(1, 1), b3 + hstep, voffB);
;             PG8_WAIT_V(6); PG8_BAR; PG8_MMA(1, 1, At, B1); PG8_BAR;
;             }
;         }
;         if constexpr (ALIGN_EPI) { if (wr == 0) PG8_BAR; }
	s_add_u32 s48, s24, 0x80
	s_addc_u32 s49, s25, 0
	ds_read_b128 v[174:177], v149 offset:49152
	ds_read_b128 v[178:181], v149 offset:50176
	ds_read_b128 v[182:185], v149 offset:51200
	ds_read_b128 v[186:189], v149 offset:52224
	ds_read_b128 v[190:193], v149 offset:53248
	ds_read_b128 v[194:197], v149 offset:54272
	ds_read_b128 v[198:201], v149 offset:55296
	ds_read_b128 v[202:205], v149 offset:56320
	s_add_i32 s47, s47, s28
	v_lshl_add_u64 v[146:147], s[48:49], 0, v[112:113]
	s_add_u32 s48, s24, 0x10080
	s_mov_b32 m0, s47
	s_addc_u32 s49, s25, 0
	global_load_lds_dwordx4 v[146:147], off
	s_add_i32 m0, s47, 0x2000
	v_lshl_add_u64 v[146:147], s[48:49], 0, v[112:113]
	s_add_u32 s48, s24, 0x20080
	s_addc_u32 s49, s25, 0
	s_add_i32 s47, s50, s28
	global_load_lds_dwordx4 v[146:147], off
	s_mov_b32 m0, s47
	v_lshl_add_u64 v[146:147], s[48:49], 0, v[112:113]
	s_add_u32 s24, s24, 0x30080
	global_load_lds_dwordx4 v[146:147], off
	s_addc_u32 s25, s25, 0
	s_add_i32 m0, s47, 0x2000
	s_add_u32 s20, s20, 0x10080
	v_lshl_add_u64 v[146:147], s[24:25], 0, v[112:113]
	global_load_lds_dwordx4 v[146:147], off
	s_mov_b32 m0, s43
	v_lshl_add_u64 v[146:147], s[22:23], 0, v[130:131]
	s_addc_u32 s21, s21, 0
	global_load_lds_dwordx4 v[146:147], off
	s_mov_b32 m0, s44
	v_lshl_add_u64 v[146:147], s[20:21], 0, v[130:131]
	global_load_lds_dwordx4 v[146:147], off
	s_waitcnt vmcnt(8)
	s_waitcnt lgkmcnt(0)
	s_barrier
	s_setprio 1
	s_waitcnt lgkmcnt(0)
	v_mfma_i32_16x16x64_i8 v[60:63], v[132:135], v[174:177], v[60:63]
	v_mfma_i32_16x16x64_i8 v[52:55], v[142:145], v[174:177], v[52:55]
	v_mfma_i32_16x16x64_i8 v[44:47], v[132:135], v[182:185], v[44:47]
	v_mfma_i32_16x16x64_i8 v[36:39], v[142:145], v[182:185], v[36:39]
	v_mfma_i32_16x16x64_i8 v[28:31], v[132:135], v[190:193], v[28:31]
	v_mfma_i32_16x16x64_i8 v[20:23], v[142:145], v[190:193], v[20:23]
	v_mfma_i32_16x16x64_i8 v[12:15], v[132:135], v[198:201], v[12:15]
	v_mfma_i32_16x16x64_i8 v[4:7], v[142:145], v[198:201], v[4:7]
	v_mfma_i32_16x16x64_i8 v[60:63], v[138:141], v[178:181], v[60:63]
	v_mfma_i32_16x16x64_i8 v[52:55], v[150:153], v[178:181], v[52:55]
	v_mfma_i32_16x16x64_i8 v[44:47], v[138:141], v[186:189], v[44:47]
	v_mfma_i32_16x16x64_i8 v[36:39], v[150:153], v[186:189], v[36:39]
	v_mfma_i32_16x16x64_i8 v[28:31], v[138:141], v[194:197], v[28:31]
	v_mfma_i32_16x16x64_i8 v[20:23], v[150:153], v[194:197], v[20:23]
	v_mfma_i32_16x16x64_i8 v[12:15], v[138:141], v[202:205], v[12:15]
	v_mfma_i32_16x16x64_i8 v[4:7], v[150:153], v[202:205], v[4:7]
	v_mfma_i32_16x16x64_i8 v[56:59], v[154:157], v[174:177], v[56:59]
	v_mfma_i32_16x16x64_i8 v[48:51], v[166:169], v[174:177], v[48:51]
	v_mfma_i32_16x16x64_i8 v[40:43], v[154:157], v[182:185], v[40:43]
	v_mfma_i32_16x16x64_i8 v[32:35], v[166:169], v[182:185], v[32:35]
	v_mfma_i32_16x16x64_i8 v[24:27], v[154:157], v[190:193], v[24:27]
	v_mfma_i32_16x16x64_i8 v[16:19], v[166:169], v[190:193], v[16:19]
	v_mfma_i32_16x16x64_i8 v[8:11], v[154:157], v[198:201], v[8:11]
	v_mfma_i32_16x16x64_i8 v[0:3], v[166:169], v[198:201], v[0:3]
	v_mfma_i32_16x16x64_i8 v[56:59], v[158:161], v[178:181], v[56:59]
	v_mfma_i32_16x16x64_i8 v[48:51], v[170:173], v[178:181], v[48:51]
	v_mfma_i32_16x16x64_i8 v[40:43], v[158:161], v[186:189], v[40:43]
	v_mfma_i32_16x16x64_i8 v[32:35], v[170:173], v[186:189], v[32:35]
	v_mfma_i32_16x16x64_i8 v[24:27], v[158:161], v[194:197], v[24:27]
	v_mfma_i32_16x16x64_i8 v[16:19], v[170:173], v[194:197], v[16:19]
	v_mfma_i32_16x16x64_i8 v[8:11], v[158:161], v[202:205], v[8:11]
	v_mfma_i32_16x16x64_i8 v[0:3], v[170:173], v[202:205], v[0:3]
	s_setprio 0
	s_barrier
	s_add_i32 s46, s46, 2
	s_add_u32 s9, s9, 0x100
	s_addc_u32 s11, s11, 0
	s_add_u32 s18, s18, 0x100
	s_addc_u32 s19, s19, 0
	s_cmp_gt_u32 s46, 5
	s_cbranch_scc0 .LBB0_1767
	s_and_b64 vcc, exec, s[4:5]
	s_cbranch_vccz .LBB0_1770
	s_barrier
